# out-projection GEMMs (both layers): first K-tile of every unit peeled with C = 0, accumulator-zeroing moves removed
# baseline (speedup 1.0000x reference)
; #define LAS __attribute__((address_space(3)))
; #define PG8_STAGE(bufoff, gbase, voff) do { _Pragma("unroll") for (int _i = 0; _i < 2; ++_i) \
;         __builtin_amdgcn_global_load_lds((const unsigned*)((const char*)(gbase) + (voff)[_i]), (LAS unsigned*)(lds + (bufoff) + ldsw + _i * 8192), 16, 0, 0); } while (0)
; #define PG8_STAGEA(bufoff, h, ap, kb, go) do { if constexpr (GATHER) { PG8_STAGE(bufoff, (const char*)g.A + (kb), go[h]); } else { PG8_STAGE(bufoff, (ap) + (h) * hstep, voffA); } } while (0)
; #define PG8_WAIT_V(n) asm volatile("s_waitcnt vmcnt(" #n ")" ::: "memory")
; #define PG8_WAIT_L(n) asm volatile("s_waitcnt lgkmcnt(" #n ")" ::: "memory")
; #define PG8_BAR __builtin_amdgcn_s_barrier()
; template <class Epi, class Sched, bool GATHER, bool FP8 = false>
; __device__ __forceinline__ void gemm_phase(LAS unsigned char* lds, LAS int* idx, const Gemm g, const Sched& S, const Epi& E) {
;     ...
;     f32x4 acc[2][2][4][2];
; #pragma unroll
;     for (int a = 0; a < 2; ++a)
; #pragma unroll
;         for (int b = 0; b < 2; ++b)
; #pragma unroll
;             for (int m = 0; m < 4; ++m)
; #pragma unroll
;                 for (int n = 0; n < 2; ++n) acc[a][b][m][n] = (f32x4){0.f, 0.f, 0.f, 0.f};
;     bf16x8 At[4][2], B0[2][2], B1[2][2]; i32x8 At8[4], B08[2], B18[2];
;     const unsigned epi_scale = 0x01010101u * (unsigned)(127 + Epi::SEXP);
;     const unsigned one_scale = 0x7f7f7f7fu;
;     const char* cA = (const char*)g.A + (GATHER ? (size_t)0 : (size_t)cur.pm * tstep + (size_t)cur.be * g.astride);
;     const char* cB = (const char*)g.Bt + (size_t)cur.be * g.bstride + (size_t)cur.pn * tstep;
;     unsigned gc[2][2] = {{0u, 0u}, {0u, 0u}};
;     ...
;     if constexpr (GATHER) {
;         if (wid == 0) __builtin_amdgcn_global_load_lds((const unsigned*)(g.gather + (size_t)cur.pm * BM + lane * 4), (LAS unsigned*)idx, 16, 0, 0);
;         PG8_WAIT_V(0); PG8_BAR;
;         PG8_GIDX(gc, 0);
;         PG8_WAIT_L(0); PG8_BAR;
;     }
;     PG8_STAGE(PG8_SB(0, 0), cB, voffB); PG8_STAGE(PG8_SB(0, 1), cB + hstepB, voffB); PG8_STAGEA(PG8_SA(0, 0), 0, cA, 0, gc); PG8_STAGEA(PG8_SA(0, 1), 1, cA, 0, gc);
;     if (wr == 1) PG8_BAR;
;     PG8_WAIT_V(2); PG8_BAR;
;     PG8_STAGE(PG8_SB(1, 0), cB + kstep, voffB); PG8_STAGEA(PG8_SA(1, 0), 0, cA + kstep, kstep, gc); PG8_STAGE(PG8_SB(1, 1), cB + hstepB + kstep, voffB);
;     PG8_WAIT_V(6); PG8_BAR;
;     for (;;) {
.LBB0_451:
	s_cmp_lg_u32 s26, 0
	s_cselect_b64 s[26:27], -1, 0
	s_add_u32 s65, s28, 0x100
	s_mov_b32 s64, 0
	s_addc_u32 s66, s29, 0
	v_lshl_add_u64 v[210:211], s[24:25], 0, v[202:203]
	v_lshl_add_u64 v[212:213], s[24:25], 0, v[204:205]
	s_mov_b64 s[28:29], 0
	s_branch .Lpl453_453

; #define PG8_STAGE(bufoff, gbase, voff) do { _Pragma("unroll") for (int _i = 0; _i < 2; ++_i) \
;         __builtin_amdgcn_global_load_lds((const unsigned*)((const char*)(gbase) + (voff)[_i]), (LAS unsigned*)(lds + (bufoff) + ldsw + _i * 8192), 16, 0, 0); } while (0)
; #define PG8_STAGEA(bufoff, h, ap, kb, go) do { if constexpr (GATHER) { PG8_STAGE(bufoff, (const char*)g.A + (kb), go[h]); } else { PG8_STAGE(bufoff, (ap) + (h) * hstep, voffA); } } while (0)
; #define PG8_WAIT_V(n) asm volatile("s_waitcnt vmcnt(" #n ")" ::: "memory")
; #define PG8_WAIT_L(n) asm volatile("s_waitcnt lgkmcnt(" #n ")" ::: "memory")
; #define PG8_BAR __builtin_amdgcn_s_barrier()
; #define PG8_SCHED __builtin_amdgcn_sched_barrier(0)
; template <class Epi, class Sched, bool GATHER, bool FP8 = false>
; __device__ __forceinline__ void gemm_phase(LAS unsigned char* lds, LAS int* idx, const Gemm g, const Sched& S, const Epi& E) {
;     ...
;             PG8_LDB(B0, 1, 0); PG8_LDB(B1, 1, 1); PG8_SCHED; PG8_LDA(At, 1, 0); PG8_STAGEA(PG8_SA(0, 1), 1, a2, k2, g2);
;             PG8_WAIT_V(8); PG8_WAIT_L(0); PG8_BAR; PG8_MMA(0, 0, At, B0); PG8_MMA(0, 1, At, B1); PG8_BAR; PG8_SCHED;
;             PG8_LDA(At, 1, 1); PG8_STAGE(PG8_SB(1, 0), b3, voffB); PG8_STAGE(PG8_SB(1, 1), b3 + hstepB, voffB); PG8_STAGEA(PG8_SA(1, 0), 0, a3, k3, g2);
;             PG8_WAIT_V(8); PG8_WAIT_L(0); PG8_BAR; PG8_MMA(1, 0, At, B0); PG8_MMA(1, 1, At, B1); PG8_BAR; PG8_SCHED;
;             if constexpr (GATHER) { if (last) { _Pragma("unroll") for (int h = 0; h < 2; ++h) _Pragma("unroll") for (int i = 0; i < 2; ++i) gc[h][i] = g2[h][i]; } }
;             t += 2;
;         } while (t < nt);
.Lpl453_join:
	s_setprio 0
	s_barrier
	ds_read_b128 v[2:5], v235
	ds_read_b128 v[6:9], v236
	ds_read_b128 v[10:13], v237
	ds_read_b128 v[14:17], v238
	ds_read_b128 v[18:21], v239
	ds_read_b128 v[22:25], v240
	ds_read_b128 v[26:29], v241
	ds_read_b128 v[30:33], v242
	s_add_u32 s30, s30, s2
	s_addc_u32 s31, s31, s3
	s_mov_b32 m0, s45
	v_lshl_add_u64 v[246:247], s[30:31], 0, v[194:195]
	ds_read_b128 v[34:37], v244 offset:32768
	ds_read_b128 v[38:41], v244 offset:33792
	ds_read_b128 v[42:45], v244 offset:34816
	ds_read_b128 v[46:49], v244 offset:35840
	ds_read_b128 v[50:53], v244 offset:36864
	ds_read_b128 v[54:57], v244 offset:37888
	ds_read_b128 v[58:61], v244 offset:38912
	ds_read_b128 v[62:65], v244 offset:39936
	global_load_lds_dwordx4 v[246:247], off
	v_lshl_add_u64 v[246:247], s[30:31], 0, v[198:199]
	s_mov_b32 m0, s46
	s_nop 0
	global_load_lds_dwordx4 v[246:247], off
	s_waitcnt vmcnt(8)
	s_waitcnt lgkmcnt(0)
	s_barrier
	s_setprio 1
	s_waitcnt lgkmcnt(0)
	v_mfma_scale_f32_16x16x128_f8f6f4 v[190:193], v[2:9], v[34:41], v[190:193], v245, v245 op_sel_hi:[0,0,0]
	v_mfma_scale_f32_16x16x128_f8f6f4 v[186:189], v[10:17], v[34:41], v[186:189], v245, v245 op_sel_hi:[0,0,0]
	v_mfma_scale_f32_16x16x128_f8f6f4 v[174:177], v[2:9], v[42:49], v[174:177], v245, v245 op_sel_hi:[0,0,0]
	v_mfma_scale_f32_16x16x128_f8f6f4 v[170:173], v[10:17], v[42:49], v[170:173], v245, v245 op_sel_hi:[0,0,0]
	v_mfma_scale_f32_16x16x128_f8f6f4 v[158:161], v[2:9], v[50:57], v[158:161], v245, v245 op_sel_hi:[0,0,0]
	v_mfma_scale_f32_16x16x128_f8f6f4 v[154:157], v[10:17], v[50:57], v[154:157], v245, v245 op_sel_hi:[0,0,0]
	v_mfma_scale_f32_16x16x128_f8f6f4 v[142:145], v[2:9], v[58:65], v[142:145], v245, v245 op_sel_hi:[0,0,0]
	v_mfma_scale_f32_16x16x128_f8f6f4 v[138:141], v[10:17], v[58:65], v[138:141], v245, v245 op_sel_hi:[0,0,0]
	s_setprio 0
	s_setprio 1
	v_mfma_scale_f32_16x16x128_f8f6f4 v[182:185], v[18:25], v[34:41], v[182:185], v245, v245 op_sel_hi:[0,0,0]
	v_mfma_scale_f32_16x16x128_f8f6f4 v[178:181], v[26:33], v[34:41], v[178:181], v245, v245 op_sel_hi:[0,0,0]
	v_mfma_scale_f32_16x16x128_f8f6f4 v[166:169], v[18:25], v[42:49], v[166:169], v245, v245 op_sel_hi:[0,0,0]
	v_mfma_scale_f32_16x16x128_f8f6f4 v[162:165], v[26:33], v[42:49], v[162:165], v245, v245 op_sel_hi:[0,0,0]
	v_mfma_scale_f32_16x16x128_f8f6f4 v[150:153], v[18:25], v[50:57], v[150:153], v245, v245 op_sel_hi:[0,0,0]
	v_mfma_scale_f32_16x16x128_f8f6f4 v[146:149], v[26:33], v[50:57], v[146:149], v245, v245 op_sel_hi:[0,0,0]
	v_mfma_scale_f32_16x16x128_f8f6f4 v[134:137], v[18:25], v[58:65], v[134:137], v245, v245 op_sel_hi:[0,0,0]
	v_mfma_scale_f32_16x16x128_f8f6f4 v[130:133], v[26:33], v[58:65], v[130:133], v245, v245 op_sel_hi:[0,0,0]
	s_setprio 0
	s_barrier
	s_mov_b32 m0, s49
	v_lshl_add_u64 v[214:215], v[214:215], 0, s[14:15]
	ds_read_b128 v[34:37], v244 offset:49152
	ds_read_b128 v[38:41], v244 offset:50176
	ds_read_b128 v[42:45], v244 offset:51200
	ds_read_b128 v[46:49], v244 offset:52224
	ds_read_b128 v[50:53], v244 offset:53248
	ds_read_b128 v[54:57], v244 offset:54272
	ds_read_b128 v[58:61], v244 offset:55296
	ds_read_b128 v[62:65], v244 offset:56320
	global_load_lds_dwordx4 v[214:215], off
	v_lshl_add_u64 v[214:215], v[216:217], 0, s[14:15]
	s_mov_b32 m0, s50
	s_nop 0
	global_load_lds_dwordx4 v[214:215], off
	v_lshl_add_u64 v[214:215], v[218:219], 0, s[14:15]
	s_mov_b32 m0, s53
	s_nop 0
	global_load_lds_dwordx4 v[214:215], off
	v_lshl_add_u64 v[214:215], v[220:221], 0, s[14:15]
	s_mov_b32 m0, s54
	s_nop 0
	global_load_lds_dwordx4 v[214:215], off
	v_lshl_add_u64 v[214:215], v[222:223], 0, s[14:15]
	s_mov_b32 m0, s51
	s_nop 0
	global_load_lds_dwordx4 v[214:215], off
	v_lshl_add_u64 v[214:215], v[224:225], 0, s[14:15]
	s_mov_b32 m0, s52
	s_nop 0
	global_load_lds_dwordx4 v[214:215], off
	s_waitcnt vmcnt(8)
	s_waitcnt lgkmcnt(0)
	s_barrier
	s_setprio 1
	s_waitcnt lgkmcnt(0)
	v_mfma_scale_f32_16x16x128_f8f6f4 v[126:129], v[2:9], v[34:41], v[126:129], v245, v245 op_sel_hi:[0,0,0]
	v_mfma_scale_f32_16x16x128_f8f6f4 v[122:125], v[10:17], v[34:41], v[122:125], v245, v245 op_sel_hi:[0,0,0]
	v_mfma_scale_f32_16x16x128_f8f6f4 v[110:113], v[2:9], v[42:49], v[110:113], v245, v245 op_sel_hi:[0,0,0]
	v_mfma_scale_f32_16x16x128_f8f6f4 v[106:109], v[10:17], v[42:49], v[106:109], v245, v245 op_sel_hi:[0,0,0]
	v_mfma_scale_f32_16x16x128_f8f6f4 v[94:97], v[2:9], v[50:57], v[94:97], v245, v245 op_sel_hi:[0,0,0]
	v_mfma_scale_f32_16x16x128_f8f6f4 v[90:93], v[10:17], v[50:57], v[90:93], v245, v245 op_sel_hi:[0,0,0]
	v_mfma_scale_f32_16x16x128_f8f6f4 v[78:81], v[2:9], v[58:65], v[78:81], v245, v245 op_sel_hi:[0,0,0]
	v_mfma_scale_f32_16x16x128_f8f6f4 v[74:77], v[10:17], v[58:65], v[74:77], v245, v245 op_sel_hi:[0,0,0]
	s_setprio 0
	s_setprio 1
	v_mfma_scale_f32_16x16x128_f8f6f4 v[118:121], v[18:25], v[34:41], v[118:121], v245, v245 op_sel_hi:[0,0,0]
	v_mfma_scale_f32_16x16x128_f8f6f4 v[114:117], v[26:33], v[34:41], v[114:117], v245, v245 op_sel_hi:[0,0,0]
	v_mfma_scale_f32_16x16x128_f8f6f4 v[102:105], v[18:25], v[42:49], v[102:105], v245, v245 op_sel_hi:[0,0,0]
	v_mfma_scale_f32_16x16x128_f8f6f4 v[98:101], v[26:33], v[42:49], v[98:101], v245, v245 op_sel_hi:[0,0,0]
	v_mfma_scale_f32_16x16x128_f8f6f4 v[86:89], v[18:25], v[50:57], v[86:89], v245, v245 op_sel_hi:[0,0,0]
	v_mfma_scale_f32_16x16x128_f8f6f4 v[82:85], v[26:33], v[50:57], v[82:85], v245, v245 op_sel_hi:[0,0,0]
	v_mfma_scale_f32_16x16x128_f8f6f4 v[70:73], v[18:25], v[58:65], v[70:73], v245, v245 op_sel_hi:[0,0,0]
	v_mfma_scale_f32_16x16x128_f8f6f4 v[66:69], v[26:33], v[58:65], v[66:69], v245, v245 op_sel_hi:[0,0,0]
	s_setprio 0
	s_barrier
	s_add_u32 s28, s28, 0x100
	s_addc_u32 s29, s29, 0
	s_cmp_lt_i32 s64, s55
	s_cbranch_scc0 .LBB0_461

; #define PG8_STAGEA(bufoff, h, ap, kb, go) do { if constexpr (GATHER) { PG8_STAGE(bufoff, (const char*)g.A + (kb), go[h]); } else { PG8_STAGE(bufoff, (ap) + (h) * hstep, voffA); } } while (0)
; #define PG8_WAIT_L(n) asm volatile("s_waitcnt lgkmcnt(" #n ")" ::: "memory")
; #define PG8_WAIT_V8R() do { if (relax) { if (GATHER && wid == 0 && has_next) asm volatile("s_waitcnt vmcnt(%0)" :: "n"(9 + Epi::NSTORES) : "memory"); else asm volatile("s_waitcnt vmcnt(%0)" :: "n"(8 + Epi::NSTORES) : "memory"); } else PG8_WAIT_V(8); } while (0)
; #define PG8_BAR __builtin_amdgcn_s_barrier()
; #define PG8_SCHED __builtin_amdgcn_sched_barrier(0)
; template <class Epi, class Sched, bool GATHER, bool FP8 = false>
; __device__ __forceinline__ void gemm_phase(LAS unsigned char* lds, LAS int* idx, const Gemm g, const Sched& S, const Epi& E) {
;     ...
;             const int relax = __builtin_amdgcn_readfirstlane(((t == 0) && (ui > 0)) ? 1 : 0);
;             PG8_LDB(B0, 0, 0); PG8_LDB(B1, 0, 1); PG8_SCHED; PG8_LDA(At, 0, 0); PG8_STAGEA(PG8_SA(1, 1), 1, a1, k1, gc);
;             PG8_WAIT_V8R(); PG8_WAIT_L(0); PG8_BAR; PG8_MMA(0, 0, At, B0); PG8_MMA(0, 1, At, B1); PG8_BAR; PG8_SCHED;
.LBB0_459:
	s_andn2_b64 vcc, exec, s[36:37]
	s_cbranch_vccnz .LBB0_452
	s_waitcnt vmcnt(24)
	s_branch .LBB0_452
.Lpl453_453:
	ds_read_b128 v[26:29], v226
	ds_read_b128 v[30:33], v227
	ds_read_b128 v[18:21], v228
	ds_read_b128 v[22:25], v229
	ds_read_b128 v[10:13], v231
	ds_read_b128 v[14:17], v232
	ds_read_b128 v[2:5], v233
	ds_read_b128 v[6:9], v234
	s_cmp_eq_u32 s64, 0
	s_cselect_b64 s[30:31], -1, 0
	s_and_b64 s[30:31], s[26:27], s[30:31]
	v_lshl_add_u64 v[214:215], v[210:211], 0, s[28:29]
	s_add_i32 m0, s39, 0xc000
	ds_read_b128 v[58:61], v244
	ds_read_b128 v[62:65], v244 offset:1024
	ds_read_b128 v[50:53], v244 offset:2048
	ds_read_b128 v[54:57], v244 offset:3072
	ds_read_b128 v[42:45], v244 offset:4096
	ds_read_b128 v[46:49], v244 offset:5120
	ds_read_b128 v[34:37], v244 offset:6144
	ds_read_b128 v[38:41], v244 offset:7168
	global_load_lds_dwordx4 v[214:215], off
	v_lshl_add_u64 v[214:215], v[212:213], 0, s[28:29]
	s_add_i32 m0, s39, 0xe000
	s_nop 0
	global_load_lds_dwordx4 v[214:215], off
	s_and_b64 vcc, exec, s[30:31]
	s_not_b64 s[34:35], s[30:31]
	s_mov_b64 s[30:31], -1
	s_cbranch_vccnz .Lpl453_455
	s_waitcnt vmcnt(8)
	s_mov_b64 s[30:31], 0

; #define PG8_STAGE(bufoff, gbase, voff) do { _Pragma("unroll") for (int _i = 0; _i < 2; ++_i) \
;         __builtin_amdgcn_global_load_lds((const unsigned*)((const char*)(gbase) + (voff)[_i]), (LAS unsigned*)(lds + (bufoff) + ldsw + _i * 8192), 16, 0, 0); } while (0)
; #define PG8_STAGEA(bufoff, h, ap, kb, go) do { if constexpr (GATHER) { PG8_STAGE(bufoff, (const char*)g.A + (kb), go[h]); } else { PG8_STAGE(bufoff, (ap) + (h) * hstep, voffA); } } while (0)
; #define PG8_WAIT_L(n) asm volatile("s_waitcnt lgkmcnt(" #n ")" ::: "memory")
; #define PG8_WAIT_V8R() do { if (relax) { if (GATHER && wid == 0 && has_next) asm volatile("s_waitcnt vmcnt(%0)" :: "n"(9 + Epi::NSTORES) : "memory"); else asm volatile("s_waitcnt vmcnt(%0)" :: "n"(8 + Epi::NSTORES) : "memory"); } else PG8_WAIT_V(8); } while (0)
; #define PG8_BAR __builtin_amdgcn_s_barrier()
; template <class Epi, class Sched, bool GATHER, bool FP8 = false>
; __device__ __forceinline__ void gemm_phase(LAS unsigned char* lds, LAS int* idx, const Gemm g, const Sched& S, const Epi& E) {
;     ...
;             const bool last = (t == nt - 2);
;             const char* a1 = cA + (size_t)(t + 1) * kstep;
;             const char* a2 = last ? nA : cA + (size_t)(t + 2) * kstep; const char* b2 = last ? nB : cB + (size_t)(t + 2) * kstep;
;             const char* a3 = a2 + kstep; const char* b3 = b2 + kstep;
;             const size_t k1 = (size_t)(t + 1) * kstep, k2 = last ? (size_t)0 : (size_t)(t + 2) * kstep, k3 = k2 + kstep;
;             unsigned g2[2][2];
; #pragma unroll
;             for (int h = 0; h < 2; ++h)
; #pragma unroll
;                 for (int i = 0; i < 2; ++i) g2[h][i] = gc[h][i];
;             if constexpr (GATHER) { if (last && has_next) PG8_GIDX(g2, ((ui + 1) & 1) * BM); }
;             const int relax = __builtin_amdgcn_readfirstlane(((t == 0) && (ui > 0)) ? 1 : 0);
;             PG8_LDB(B0, 0, 0); PG8_LDB(B1, 0, 1); PG8_SCHED; PG8_LDA(At, 0, 0); PG8_STAGEA(PG8_SA(1, 1), 1, a1, k1, gc);
;             PG8_WAIT_V8R(); PG8_WAIT_L(0); PG8_BAR; PG8_MMA(0, 0, At, B0); PG8_MMA(0, 1, At, B1); PG8_BAR; PG8_SCHED;
;             PG8_LDA(At, 0, 1); PG8_STAGE(PG8_SB(0, 0), b2, voffB); PG8_STAGE(PG8_SB(0, 1), b2 + hstepB, voffB); PG8_STAGEA(PG8_SA(0, 0), 0, a2, k2, g2);
;             PG8_WAIT_V8R(); PG8_WAIT_L(0); PG8_BAR; PG8_MMA(1, 0, At, B0); PG8_MMA(1, 1, At, B1); PG8_BAR; PG8_SCHED;
.Lpl453_457:
	s_add_u32 s30, s24, s28
	s_addc_u32 s31, s25, s29
	s_add_u32 s30, s30, 0x100
	s_addc_u32 s31, s31, 0
	s_add_u32 s36, s65, s28
	s_addc_u32 s37, s66, s29
	s_waitcnt lgkmcnt(0)
	s_cmp_eq_u32 s56, s64
	s_cselect_b32 s31, s9, s31
	s_cselect_b32 s30, s8, s30
	s_cselect_b32 s37, s23, s37
	s_cselect_b32 s36, s22, s36
	s_barrier
	s_setprio 1
	s_waitcnt lgkmcnt(0)
	v_mfma_scale_f32_16x16x128_f8f6f4 v[190:193], v[26:33], v[58:65], 0, v245, v245 op_sel_hi:[0,0,0]
	v_mfma_scale_f32_16x16x128_f8f6f4 v[186:189], v[18:25], v[58:65], 0, v245, v245 op_sel_hi:[0,0,0]
	v_mfma_scale_f32_16x16x128_f8f6f4 v[174:177], v[26:33], v[50:57], 0, v245, v245 op_sel_hi:[0,0,0]
	v_mfma_scale_f32_16x16x128_f8f6f4 v[170:173], v[18:25], v[50:57], 0, v245, v245 op_sel_hi:[0,0,0]
	v_mfma_scale_f32_16x16x128_f8f6f4 v[158:161], v[26:33], v[42:49], 0, v245, v245 op_sel_hi:[0,0,0]
	v_mfma_scale_f32_16x16x128_f8f6f4 v[154:157], v[18:25], v[42:49], 0, v245, v245 op_sel_hi:[0,0,0]
	v_mfma_scale_f32_16x16x128_f8f6f4 v[142:145], v[26:33], v[34:41], 0, v245, v245 op_sel_hi:[0,0,0]
	v_mfma_scale_f32_16x16x128_f8f6f4 v[138:141], v[18:25], v[34:41], 0, v245, v245 op_sel_hi:[0,0,0]
	s_setprio 0
	s_setprio 1
	v_mfma_scale_f32_16x16x128_f8f6f4 v[182:185], v[10:17], v[58:65], 0, v245, v245 op_sel_hi:[0,0,0]
	v_mfma_scale_f32_16x16x128_f8f6f4 v[178:181], v[2:9], v[58:65], 0, v245, v245 op_sel_hi:[0,0,0]
	v_mfma_scale_f32_16x16x128_f8f6f4 v[166:169], v[10:17], v[50:57], 0, v245, v245 op_sel_hi:[0,0,0]
	v_mfma_scale_f32_16x16x128_f8f6f4 v[162:165], v[2:9], v[50:57], 0, v245, v245 op_sel_hi:[0,0,0]
	v_mfma_scale_f32_16x16x128_f8f6f4 v[150:153], v[10:17], v[42:49], 0, v245, v245 op_sel_hi:[0,0,0]
	v_mfma_scale_f32_16x16x128_f8f6f4 v[146:149], v[2:9], v[42:49], 0, v245, v245 op_sel_hi:[0,0,0]
	v_mfma_scale_f32_16x16x128_f8f6f4 v[134:137], v[10:17], v[34:41], 0, v245, v245 op_sel_hi:[0,0,0]
	v_mfma_scale_f32_16x16x128_f8f6f4 v[130:133], v[2:9], v[34:41], 0, v245, v245 op_sel_hi:[0,0,0]
	s_setprio 0
	s_barrier
	s_mov_b32 m0, s40
	v_lshl_add_u64 v[214:215], s[36:37], 0, v[196:197]
	v_lshl_add_u64 v[216:217], s[36:37], 0, v[200:201]
	s_add_u32 s36, s36, s10
	ds_read_b128 v[58:61], v244 offset:16384
	ds_read_b128 v[62:65], v244 offset:17408
	ds_read_b128 v[50:53], v244 offset:18432
	ds_read_b128 v[54:57], v244 offset:19456
	ds_read_b128 v[42:45], v244 offset:20480
	ds_read_b128 v[46:49], v244 offset:21504
	ds_read_b128 v[34:37], v244 offset:22528
	ds_read_b128 v[38:41], v244 offset:23552
	global_load_lds_dwordx4 v[214:215], off
	s_mov_b32 m0, s41
	s_addc_u32 s37, s37, s11
	global_load_lds_dwordx4 v[216:217], off
	v_lshl_add_u64 v[218:219], s[36:37], 0, v[196:197]
	s_mov_b32 m0, s42
	v_lshl_add_u64 v[220:221], s[36:37], 0, v[200:201]
	global_load_lds_dwordx4 v[218:219], off
	s_mov_b32 m0, s43
	v_lshl_add_u64 v[222:223], s[30:31], 0, v[194:195]
	global_load_lds_dwordx4 v[220:221], off
	s_mov_b32 m0, s39
	v_lshl_add_u64 v[224:225], s[30:31], 0, v[198:199]
	global_load_lds_dwordx4 v[222:223], off
	s_mov_b32 m0, s44
	s_mov_b64 s[36:37], -1
	global_load_lds_dwordx4 v[224:225], off
	s_and_b64 vcc, exec, s[34:35]
	s_cbranch_vccz .Lpl453_459
	s_waitcnt vmcnt(8)
	s_mov_b64 s[36:37], 0

; #define PG8_STAGE(bufoff, gbase, voff) do { _Pragma("unroll") for (int _i = 0; _i < 2; ++_i) \
;         __builtin_amdgcn_global_load_lds((const unsigned*)((const char*)(gbase) + (voff)[_i]), (LAS unsigned*)(lds + (bufoff) + ldsw + _i * 8192), 16, 0, 0); } while (0)
; #define PG8_STAGEA(bufoff, h, ap, kb, go) do { if constexpr (GATHER) { PG8_STAGE(bufoff, (const char*)g.A + (kb), go[h]); } else { PG8_STAGE(bufoff, (ap) + (h) * hstep, voffA); } } while (0)
; #define PG8_WAIT_V(n) asm volatile("s_waitcnt vmcnt(" #n ")" ::: "memory")
; #define PG8_WAIT_L(n) asm volatile("s_waitcnt lgkmcnt(" #n ")" ::: "memory")
; #define PG8_WAIT_V8R() do { if (relax) { if (GATHER && wid == 0 && has_next) asm volatile("s_waitcnt vmcnt(%0)" :: "n"(9 + Epi::NSTORES) : "memory"); else asm volatile("s_waitcnt vmcnt(%0)" :: "n"(8 + Epi::NSTORES) : "memory"); } else PG8_WAIT_V(8); } while (0)
; #define PG8_BAR __builtin_amdgcn_s_barrier()
; #define PG8_SCHED __builtin_amdgcn_sched_barrier(0)
; template <class Epi, class Sched, bool GATHER, bool FP8 = false>
; __device__ __forceinline__ void gemm_phase(LAS unsigned char* lds, LAS int* idx, const Gemm g, const Sched& S, const Epi& E) {
;     ...
;             PG8_WAIT_V8R(); PG8_WAIT_L(0); PG8_BAR; PG8_MMA(1, 0, At, B0); PG8_MMA(1, 1, At, B1); PG8_BAR; PG8_SCHED;
;             PG8_LDB(B0, 1, 0); PG8_LDB(B1, 1, 1); PG8_SCHED; PG8_LDA(At, 1, 0); PG8_STAGEA(PG8_SA(0, 1), 1, a2, k2, g2);
;             PG8_WAIT_V(8); PG8_WAIT_L(0); PG8_BAR; PG8_MMA(0, 0, At, B0); PG8_MMA(0, 1, At, B1); PG8_BAR; PG8_SCHED;
;             PG8_LDA(At, 1, 1); PG8_STAGE(PG8_SB(1, 0), b3, voffB); PG8_STAGE(PG8_SB(1, 1), b3 + hstepB, voffB); PG8_STAGEA(PG8_SA(1, 0), 0, a3, k3, g2);
;             PG8_WAIT_V(8); PG8_WAIT_L(0); PG8_BAR; PG8_MMA(1, 0, At, B0); PG8_MMA(1, 1, At, B1); PG8_BAR; PG8_SCHED;
;             if constexpr (GATHER) { if (last) { _Pragma("unroll") for (int h = 0; h < 2; ++h) _Pragma("unroll") for (int i = 0; i < 2; ++i) gc[h][i] = g2[h][i]; } }
;             t += 2;
.Lpl453_452:
	s_waitcnt lgkmcnt(0)
	s_add_i32 s64, s64, 2
	s_barrier
	s_setprio 1
	s_waitcnt lgkmcnt(0)
	v_mfma_scale_f32_16x16x128_f8f6f4 v[126:129], v[26:33], v[58:65], 0, v245, v245 op_sel_hi:[0,0,0]
	v_mfma_scale_f32_16x16x128_f8f6f4 v[122:125], v[18:25], v[58:65], 0, v245, v245 op_sel_hi:[0,0,0]
	v_mfma_scale_f32_16x16x128_f8f6f4 v[110:113], v[26:33], v[50:57], 0, v245, v245 op_sel_hi:[0,0,0]
	v_mfma_scale_f32_16x16x128_f8f6f4 v[106:109], v[18:25], v[50:57], 0, v245, v245 op_sel_hi:[0,0,0]
	v_mfma_scale_f32_16x16x128_f8f6f4 v[94:97], v[26:33], v[42:49], 0, v245, v245 op_sel_hi:[0,0,0]
	v_mfma_scale_f32_16x16x128_f8f6f4 v[90:93], v[18:25], v[42:49], 0, v245, v245 op_sel_hi:[0,0,0]
	v_mfma_scale_f32_16x16x128_f8f6f4 v[78:81], v[26:33], v[34:41], 0, v245, v245 op_sel_hi:[0,0,0]
	v_mfma_scale_f32_16x16x128_f8f6f4 v[74:77], v[18:25], v[34:41], 0, v245, v245 op_sel_hi:[0,0,0]
	s_setprio 0
	s_setprio 1
	v_mfma_scale_f32_16x16x128_f8f6f4 v[118:121], v[10:17], v[58:65], 0, v245, v245 op_sel_hi:[0,0,0]
	v_mfma_scale_f32_16x16x128_f8f6f4 v[114:117], v[2:9], v[58:65], 0, v245, v245 op_sel_hi:[0,0,0]
	v_mfma_scale_f32_16x16x128_f8f6f4 v[102:105], v[10:17], v[50:57], 0, v245, v245 op_sel_hi:[0,0,0]
	v_mfma_scale_f32_16x16x128_f8f6f4 v[98:101], v[2:9], v[50:57], 0, v245, v245 op_sel_hi:[0,0,0]
	v_mfma_scale_f32_16x16x128_f8f6f4 v[86:89], v[10:17], v[42:49], 0, v245, v245 op_sel_hi:[0,0,0]
	v_mfma_scale_f32_16x16x128_f8f6f4 v[82:85], v[2:9], v[42:49], 0, v245, v245 op_sel_hi:[0,0,0]
	v_mfma_scale_f32_16x16x128_f8f6f4 v[70:73], v[10:17], v[34:41], 0, v245, v245 op_sel_hi:[0,0,0]
	v_mfma_scale_f32_16x16x128_f8f6f4 v[66:69], v[2:9], v[34:41], 0, v245, v245 op_sel_hi:[0,0,0]
	s_branch .Lpl453_join

; #define PG8_STAGE(bufoff, gbase, voff) do { _Pragma("unroll") for (int _i = 0; _i < 2; ++_i) \
;         __builtin_amdgcn_global_load_lds((const unsigned*)((const char*)(gbase) + (voff)[_i]), (LAS unsigned*)(lds + (bufoff) + ldsw + _i * 8192), 16, 0, 0); } while (0)
; #define PG8_STAGEA(bufoff, h, ap, kb, go) do { if constexpr (GATHER) { PG8_STAGE(bufoff, (const char*)g.A + (kb), go[h]); } else { PG8_STAGE(bufoff, (ap) + (h) * hstep, voffA); } } while (0)
; #define PG8_WAIT_V(n) asm volatile("s_waitcnt vmcnt(" #n ")" ::: "memory")
; #define PG8_WAIT_L(n) asm volatile("s_waitcnt lgkmcnt(" #n ")" ::: "memory")
; #define PG8_BAR __builtin_amdgcn_s_barrier()
; #define PG8_SCHED __builtin_amdgcn_sched_barrier(0)
; template <class Epi, class Sched, bool GATHER, bool FP8 = false>
; __device__ __forceinline__ void gemm_phase(LAS unsigned char* lds, LAS int* idx, const Gemm g, const Sched& S, const Epi& E) {
;     ...
;             PG8_LDB(B0, 1, 0); PG8_LDB(B1, 1, 1); PG8_SCHED; PG8_LDA(At, 1, 0); PG8_STAGEA(PG8_SA(0, 1), 1, a2, k2, g2);
;             PG8_WAIT_V(8); PG8_WAIT_L(0); PG8_BAR; PG8_MMA(0, 0, At, B0); PG8_MMA(0, 1, At, B1); PG8_BAR; PG8_SCHED;
;             PG8_LDA(At, 1, 1); PG8_STAGE(PG8_SB(1, 0), b3, voffB); PG8_STAGE(PG8_SB(1, 1), b3 + hstepB, voffB); PG8_STAGEA(PG8_SA(1, 0), 0, a3, k3, g2);
;             PG8_WAIT_V(8); PG8_WAIT_L(0); PG8_BAR; PG8_MMA(1, 0, At, B0); PG8_MMA(1, 1, At, B1); PG8_BAR; PG8_SCHED;
;             if constexpr (GATHER) { if (last) { _Pragma("unroll") for (int h = 0; h < 2; ++h) _Pragma("unroll") for (int i = 0; i < 2; ++i) gc[h][i] = g2[h][i]; } }
;             t += 2;
;         } while (t < nt);
.Lpl1226_join:
	s_setprio 0
	s_barrier
	ds_read_b128 v[2:5], v236
	ds_read_b128 v[6:9], v237
	ds_read_b128 v[10:13], v238
	ds_read_b128 v[14:17], v239
	ds_read_b128 v[18:21], v240
	ds_read_b128 v[22:25], v241
	ds_read_b128 v[26:29], v242
	ds_read_b128 v[30:33], v243
	s_add_u32 s30, s30, s2
	s_addc_u32 s31, s31, s3
	s_mov_b32 m0, s45
	v_lshl_add_u64 v[248:249], s[30:31], 0, v[194:195]
	ds_read_b128 v[34:37], v245 offset:32768
	ds_read_b128 v[38:41], v245 offset:33792
	ds_read_b128 v[42:45], v245 offset:34816
	ds_read_b128 v[46:49], v245 offset:35840
	ds_read_b128 v[50:53], v245 offset:36864
	ds_read_b128 v[54:57], v245 offset:37888
	ds_read_b128 v[58:61], v245 offset:38912
	ds_read_b128 v[62:65], v245 offset:39936
	global_load_lds_dwordx4 v[248:249], off
	v_lshl_add_u64 v[248:249], s[30:31], 0, v[198:199]
	s_mov_b32 m0, s46
	s_nop 0
	global_load_lds_dwordx4 v[248:249], off
	s_waitcnt vmcnt(8)
	s_waitcnt lgkmcnt(0)
	s_barrier
	s_setprio 1
	s_waitcnt lgkmcnt(0)
	v_mfma_scale_f32_16x16x128_f8f6f4 v[190:193], v[2:9], v[34:41], v[190:193], v246, v246 op_sel_hi:[0,0,0]
	v_mfma_scale_f32_16x16x128_f8f6f4 v[186:189], v[10:17], v[34:41], v[186:189], v246, v246 op_sel_hi:[0,0,0]
	v_mfma_scale_f32_16x16x128_f8f6f4 v[174:177], v[2:9], v[42:49], v[174:177], v246, v246 op_sel_hi:[0,0,0]
	v_mfma_scale_f32_16x16x128_f8f6f4 v[170:173], v[10:17], v[42:49], v[170:173], v246, v246 op_sel_hi:[0,0,0]
	v_mfma_scale_f32_16x16x128_f8f6f4 v[158:161], v[2:9], v[50:57], v[158:161], v246, v246 op_sel_hi:[0,0,0]
	v_mfma_scale_f32_16x16x128_f8f6f4 v[154:157], v[10:17], v[50:57], v[154:157], v246, v246 op_sel_hi:[0,0,0]
	v_mfma_scale_f32_16x16x128_f8f6f4 v[142:145], v[2:9], v[58:65], v[142:145], v246, v246 op_sel_hi:[0,0,0]
	v_mfma_scale_f32_16x16x128_f8f6f4 v[138:141], v[10:17], v[58:65], v[138:141], v246, v246 op_sel_hi:[0,0,0]
	s_setprio 0
	s_setprio 1
	v_mfma_scale_f32_16x16x128_f8f6f4 v[182:185], v[18:25], v[34:41], v[182:185], v246, v246 op_sel_hi:[0,0,0]
	v_mfma_scale_f32_16x16x128_f8f6f4 v[178:181], v[26:33], v[34:41], v[178:181], v246, v246 op_sel_hi:[0,0,0]
	v_mfma_scale_f32_16x16x128_f8f6f4 v[166:169], v[18:25], v[42:49], v[166:169], v246, v246 op_sel_hi:[0,0,0]
	v_mfma_scale_f32_16x16x128_f8f6f4 v[162:165], v[26:33], v[42:49], v[162:165], v246, v246 op_sel_hi:[0,0,0]
	v_mfma_scale_f32_16x16x128_f8f6f4 v[150:153], v[18:25], v[50:57], v[150:153], v246, v246 op_sel_hi:[0,0,0]
	v_mfma_scale_f32_16x16x128_f8f6f4 v[146:149], v[26:33], v[50:57], v[146:149], v246, v246 op_sel_hi:[0,0,0]
	v_mfma_scale_f32_16x16x128_f8f6f4 v[134:137], v[18:25], v[58:65], v[134:137], v246, v246 op_sel_hi:[0,0,0]
	v_mfma_scale_f32_16x16x128_f8f6f4 v[130:133], v[26:33], v[58:65], v[130:133], v246, v246 op_sel_hi:[0,0,0]
	s_setprio 0
	s_barrier
	s_mov_b32 m0, s50
	v_lshl_add_u64 v[214:215], v[214:215], 0, s[14:15]
	ds_read_b128 v[34:37], v245 offset:49152
	ds_read_b128 v[38:41], v245 offset:50176
	ds_read_b128 v[42:45], v245 offset:51200
	ds_read_b128 v[46:49], v245 offset:52224
	ds_read_b128 v[50:53], v245 offset:53248
	ds_read_b128 v[54:57], v245 offset:54272
	ds_read_b128 v[58:61], v245 offset:55296
	ds_read_b128 v[62:65], v245 offset:56320
	global_load_lds_dwordx4 v[214:215], off
	v_lshl_add_u64 v[214:215], v[216:217], 0, s[14:15]
	s_mov_b32 m0, s51
	s_nop 0
	global_load_lds_dwordx4 v[214:215], off
	v_lshl_add_u64 v[214:215], v[218:219], 0, s[14:15]
	s_mov_b32 m0, s54
	s_nop 0
	global_load_lds_dwordx4 v[214:215], off
	v_lshl_add_u64 v[214:215], v[220:221], 0, s[14:15]
	s_mov_b32 m0, s55
	s_nop 0
	global_load_lds_dwordx4 v[214:215], off
	v_lshl_add_u64 v[214:215], v[222:223], 0, s[14:15]
	s_mov_b32 m0, s52
	s_nop 0
	global_load_lds_dwordx4 v[214:215], off
	v_lshl_add_u64 v[214:215], v[224:225], 0, s[14:15]
	s_mov_b32 m0, s53
	s_nop 0
	global_load_lds_dwordx4 v[214:215], off
	s_waitcnt vmcnt(8)
	s_waitcnt lgkmcnt(0)
	s_barrier
	s_setprio 1
	s_waitcnt lgkmcnt(0)
	v_mfma_scale_f32_16x16x128_f8f6f4 v[126:129], v[2:9], v[34:41], v[126:129], v246, v246 op_sel_hi:[0,0,0]
	v_mfma_scale_f32_16x16x128_f8f6f4 v[122:125], v[10:17], v[34:41], v[122:125], v246, v246 op_sel_hi:[0,0,0]
	v_mfma_scale_f32_16x16x128_f8f6f4 v[110:113], v[2:9], v[42:49], v[110:113], v246, v246 op_sel_hi:[0,0,0]
	v_mfma_scale_f32_16x16x128_f8f6f4 v[106:109], v[10:17], v[42:49], v[106:109], v246, v246 op_sel_hi:[0,0,0]
	v_mfma_scale_f32_16x16x128_f8f6f4 v[94:97], v[2:9], v[50:57], v[94:97], v246, v246 op_sel_hi:[0,0,0]
	v_mfma_scale_f32_16x16x128_f8f6f4 v[90:93], v[10:17], v[50:57], v[90:93], v246, v246 op_sel_hi:[0,0,0]
	v_mfma_scale_f32_16x16x128_f8f6f4 v[78:81], v[2:9], v[58:65], v[78:81], v246, v246 op_sel_hi:[0,0,0]
	v_mfma_scale_f32_16x16x128_f8f6f4 v[74:77], v[10:17], v[58:65], v[74:77], v246, v246 op_sel_hi:[0,0,0]
	s_setprio 0
	s_setprio 1
	v_mfma_scale_f32_16x16x128_f8f6f4 v[118:121], v[18:25], v[34:41], v[118:121], v246, v246 op_sel_hi:[0,0,0]
	v_mfma_scale_f32_16x16x128_f8f6f4 v[114:117], v[26:33], v[34:41], v[114:117], v246, v246 op_sel_hi:[0,0,0]
	v_mfma_scale_f32_16x16x128_f8f6f4 v[102:105], v[18:25], v[42:49], v[102:105], v246, v246 op_sel_hi:[0,0,0]
	v_mfma_scale_f32_16x16x128_f8f6f4 v[98:101], v[26:33], v[42:49], v[98:101], v246, v246 op_sel_hi:[0,0,0]
	v_mfma_scale_f32_16x16x128_f8f6f4 v[86:89], v[18:25], v[50:57], v[86:89], v246, v246 op_sel_hi:[0,0,0]
	v_mfma_scale_f32_16x16x128_f8f6f4 v[82:85], v[26:33], v[50:57], v[82:85], v246, v246 op_sel_hi:[0,0,0]
	v_mfma_scale_f32_16x16x128_f8f6f4 v[70:73], v[18:25], v[58:65], v[70:73], v246, v246 op_sel_hi:[0,0,0]
	v_mfma_scale_f32_16x16x128_f8f6f4 v[66:69], v[26:33], v[58:65], v[66:69], v246, v246 op_sel_hi:[0,0,0]
	s_setprio 0
	s_barrier
	s_add_u32 s28, s28, 0x100
	s_addc_u32 s29, s29, 0
	s_cmp_lt_i32 s64, s49
	s_cbranch_scc0 .LBB0_1234

; #define PG8_STAGE(bufoff, gbase, voff) do { _Pragma("unroll") for (int _i = 0; _i < 2; ++_i) \
;         __builtin_amdgcn_global_load_lds((const unsigned*)((const char*)(gbase) + (voff)[_i]), (LAS unsigned*)(lds + (bufoff) + ldsw + _i * 8192), 16, 0, 0); } while (0)
; #define PG8_STAGEA(bufoff, h, ap, kb, go) do { if constexpr (GATHER) { PG8_STAGE(bufoff, (const char*)g.A + (kb), go[h]); } else { PG8_STAGE(bufoff, (ap) + (h) * hstep, voffA); } } while (0)
; #define PG8_WAIT_L(n) asm volatile("s_waitcnt lgkmcnt(" #n ")" ::: "memory")
; #define PG8_WAIT_V8R() do { if (relax) { if (GATHER && wid == 0 && has_next) asm volatile("s_waitcnt vmcnt(%0)" :: "n"(9 + Epi::NSTORES) : "memory"); else asm volatile("s_waitcnt vmcnt(%0)" :: "n"(8 + Epi::NSTORES) : "memory"); } else PG8_WAIT_V(8); } while (0)
; #define PG8_BAR __builtin_amdgcn_s_barrier()
; #define PG8_SCHED __builtin_amdgcn_sched_barrier(0)
; template <class Epi, class Sched, bool GATHER, bool FP8 = false>
; __device__ __forceinline__ void gemm_phase(LAS unsigned char* lds, LAS int* idx, const Gemm g, const Sched& S, const Epi& E) {
;     ...
;             const int relax = __builtin_amdgcn_readfirstlane(((t == 0) && (ui > 0)) ? 1 : 0);
;             PG8_LDB(B0, 0, 0); PG8_LDB(B1, 0, 1); PG8_SCHED; PG8_LDA(At, 0, 0); PG8_STAGEA(PG8_SA(1, 1), 1, a1, k1, gc);
;             PG8_WAIT_V8R(); PG8_WAIT_L(0); PG8_BAR; PG8_MMA(0, 0, At, B0); PG8_MMA(0, 1, At, B1); PG8_BAR; PG8_SCHED;
;             PG8_LDA(At, 0, 1); PG8_STAGE(PG8_SB(0, 0), b2, voffB); PG8_STAGE(PG8_SB(0, 1), b2 + hstepB, voffB); PG8_STAGEA(PG8_SA(0, 0), 0, a2, k2, g2);
.LBB0_1232:
	s_andn2_b64 vcc, exec, s[36:37]
	s_cbranch_vccnz .LBB0_1225
	s_waitcnt vmcnt(24)
	s_branch .LBB0_1225
.Lpl1226_1226:
	ds_read_b128 v[26:29], v226
	ds_read_b128 v[30:33], v227
	ds_read_b128 v[18:21], v228
	ds_read_b128 v[22:25], v229
	ds_read_b128 v[10:13], v232
	ds_read_b128 v[14:17], v233
	ds_read_b128 v[2:5], v234
	ds_read_b128 v[6:9], v235
	s_cmp_eq_u32 s64, 0
	s_cselect_b64 s[30:31], -1, 0
	s_and_b64 s[30:31], s[26:27], s[30:31]
	v_lshl_add_u64 v[214:215], v[210:211], 0, s[28:29]
	s_add_i32 m0, s39, 0xc000
	ds_read_b128 v[58:61], v245
	ds_read_b128 v[62:65], v245 offset:1024
	ds_read_b128 v[50:53], v245 offset:2048
	ds_read_b128 v[54:57], v245 offset:3072
	ds_read_b128 v[42:45], v245 offset:4096
	ds_read_b128 v[46:49], v245 offset:5120
	ds_read_b128 v[34:37], v245 offset:6144
	ds_read_b128 v[38:41], v245 offset:7168
	global_load_lds_dwordx4 v[214:215], off
	v_lshl_add_u64 v[214:215], v[212:213], 0, s[28:29]
	s_add_i32 m0, s39, 0xe000
	s_nop 0
	global_load_lds_dwordx4 v[214:215], off
	s_and_b64 vcc, exec, s[30:31]
	s_not_b64 s[34:35], s[30:31]
	s_mov_b64 s[30:31], -1
	s_cbranch_vccnz .Lpl1226_1228
	s_waitcnt vmcnt(8)
	s_mov_b64 s[30:31], 0

; #define PG8_STAGE(bufoff, gbase, voff) do { _Pragma("unroll") for (int _i = 0; _i < 2; ++_i) \
;         __builtin_amdgcn_global_load_lds((const unsigned*)((const char*)(gbase) + (voff)[_i]), (LAS unsigned*)(lds + (bufoff) + ldsw + _i * 8192), 16, 0, 0); } while (0)
; #define PG8_STAGEA(bufoff, h, ap, kb, go) do { if constexpr (GATHER) { PG8_STAGE(bufoff, (const char*)g.A + (kb), go[h]); } else { PG8_STAGE(bufoff, (ap) + (h) * hstep, voffA); } } while (0)
; #define PG8_WAIT_L(n) asm volatile("s_waitcnt lgkmcnt(" #n ")" ::: "memory")
; #define PG8_WAIT_V8R() do { if (relax) { if (GATHER && wid == 0 && has_next) asm volatile("s_waitcnt vmcnt(%0)" :: "n"(9 + Epi::NSTORES) : "memory"); else asm volatile("s_waitcnt vmcnt(%0)" :: "n"(8 + Epi::NSTORES) : "memory"); } else PG8_WAIT_V(8); } while (0)
; #define PG8_BAR __builtin_amdgcn_s_barrier()
; template <class Epi, class Sched, bool GATHER, bool FP8 = false>
; __device__ __forceinline__ void gemm_phase(LAS unsigned char* lds, LAS int* idx, const Gemm g, const Sched& S, const Epi& E) {
;     ...
;             const bool last = (t == nt - 2);
;             const char* a1 = cA + (size_t)(t + 1) * kstep;
;             const char* a2 = last ? nA : cA + (size_t)(t + 2) * kstep; const char* b2 = last ? nB : cB + (size_t)(t + 2) * kstep;
;             const char* a3 = a2 + kstep; const char* b3 = b2 + kstep;
;             const size_t k1 = (size_t)(t + 1) * kstep, k2 = last ? (size_t)0 : (size_t)(t + 2) * kstep, k3 = k2 + kstep;
;             unsigned g2[2][2];
; #pragma unroll
;             for (int h = 0; h < 2; ++h)
; #pragma unroll
;                 for (int i = 0; i < 2; ++i) g2[h][i] = gc[h][i];
;             if constexpr (GATHER) { if (last && has_next) PG8_GIDX(g2, ((ui + 1) & 1) * BM); }
;             const int relax = __builtin_amdgcn_readfirstlane(((t == 0) && (ui > 0)) ? 1 : 0);
;             PG8_LDB(B0, 0, 0); PG8_LDB(B1, 0, 1); PG8_SCHED; PG8_LDA(At, 0, 0); PG8_STAGEA(PG8_SA(1, 1), 1, a1, k1, gc);
;             PG8_WAIT_V8R(); PG8_WAIT_L(0); PG8_BAR; PG8_MMA(0, 0, At, B0); PG8_MMA(0, 1, At, B1); PG8_BAR; PG8_SCHED;
;             PG8_LDA(At, 0, 1); PG8_STAGE(PG8_SB(0, 0), b2, voffB); PG8_STAGE(PG8_SB(0, 1), b2 + hstepB, voffB); PG8_STAGEA(PG8_SA(0, 0), 0, a2, k2, g2);
;             PG8_WAIT_V8R(); PG8_WAIT_L(0); PG8_BAR; PG8_MMA(1, 0, At, B0); PG8_MMA(1, 1, At, B1); PG8_BAR; PG8_SCHED;
.Lpl1226_1230:
	s_add_u32 s30, s24, s28
	s_addc_u32 s31, s25, s29
	s_add_u32 s30, s30, 0x100
	s_addc_u32 s31, s31, 0
	s_add_u32 s36, s65, s28
	s_addc_u32 s37, s66, s29
	s_waitcnt lgkmcnt(0)
	s_cmp_eq_u32 s56, s64
	s_cselect_b32 s31, s7, s31
	s_cselect_b32 s30, s6, s30
	s_cselect_b32 s37, s23, s37
	s_cselect_b32 s36, s22, s36
	s_barrier
	s_setprio 1
	s_waitcnt lgkmcnt(0)
	v_mfma_scale_f32_16x16x128_f8f6f4 v[190:193], v[26:33], v[58:65], 0, v246, v246 op_sel_hi:[0,0,0]
	v_mfma_scale_f32_16x16x128_f8f6f4 v[186:189], v[18:25], v[58:65], 0, v246, v246 op_sel_hi:[0,0,0]
	v_mfma_scale_f32_16x16x128_f8f6f4 v[174:177], v[26:33], v[50:57], 0, v246, v246 op_sel_hi:[0,0,0]
	v_mfma_scale_f32_16x16x128_f8f6f4 v[170:173], v[18:25], v[50:57], 0, v246, v246 op_sel_hi:[0,0,0]
	v_mfma_scale_f32_16x16x128_f8f6f4 v[158:161], v[26:33], v[42:49], 0, v246, v246 op_sel_hi:[0,0,0]
	v_mfma_scale_f32_16x16x128_f8f6f4 v[154:157], v[18:25], v[42:49], 0, v246, v246 op_sel_hi:[0,0,0]
	v_mfma_scale_f32_16x16x128_f8f6f4 v[142:145], v[26:33], v[34:41], 0, v246, v246 op_sel_hi:[0,0,0]
	v_mfma_scale_f32_16x16x128_f8f6f4 v[138:141], v[18:25], v[34:41], 0, v246, v246 op_sel_hi:[0,0,0]
	s_setprio 0
	s_setprio 1
	v_mfma_scale_f32_16x16x128_f8f6f4 v[182:185], v[10:17], v[58:65], 0, v246, v246 op_sel_hi:[0,0,0]
	v_mfma_scale_f32_16x16x128_f8f6f4 v[178:181], v[2:9], v[58:65], 0, v246, v246 op_sel_hi:[0,0,0]
	v_mfma_scale_f32_16x16x128_f8f6f4 v[166:169], v[10:17], v[50:57], 0, v246, v246 op_sel_hi:[0,0,0]
	v_mfma_scale_f32_16x16x128_f8f6f4 v[162:165], v[2:9], v[50:57], 0, v246, v246 op_sel_hi:[0,0,0]
	v_mfma_scale_f32_16x16x128_f8f6f4 v[150:153], v[10:17], v[42:49], 0, v246, v246 op_sel_hi:[0,0,0]
	v_mfma_scale_f32_16x16x128_f8f6f4 v[146:149], v[2:9], v[42:49], 0, v246, v246 op_sel_hi:[0,0,0]
	v_mfma_scale_f32_16x16x128_f8f6f4 v[134:137], v[10:17], v[34:41], 0, v246, v246 op_sel_hi:[0,0,0]
	v_mfma_scale_f32_16x16x128_f8f6f4 v[130:133], v[2:9], v[34:41], 0, v246, v246 op_sel_hi:[0,0,0]
	s_setprio 0
	s_barrier
	s_mov_b32 m0, s40
	v_lshl_add_u64 v[214:215], s[36:37], 0, v[196:197]
	v_lshl_add_u64 v[216:217], s[36:37], 0, v[200:201]
	s_add_u32 s36, s36, s8
	ds_read_b128 v[58:61], v245 offset:16384
	ds_read_b128 v[62:65], v245 offset:17408
	ds_read_b128 v[50:53], v245 offset:18432
	ds_read_b128 v[54:57], v245 offset:19456
	ds_read_b128 v[42:45], v245 offset:20480
	ds_read_b128 v[46:49], v245 offset:21504
	ds_read_b128 v[34:37], v245 offset:22528
	ds_read_b128 v[38:41], v245 offset:23552
	global_load_lds_dwordx4 v[214:215], off
	s_mov_b32 m0, s41
	s_addc_u32 s37, s37, s9
	global_load_lds_dwordx4 v[216:217], off
	v_lshl_add_u64 v[218:219], s[36:37], 0, v[196:197]
	s_mov_b32 m0, s42
	v_lshl_add_u64 v[220:221], s[36:37], 0, v[200:201]
	global_load_lds_dwordx4 v[218:219], off
	s_mov_b32 m0, s43
	v_lshl_add_u64 v[222:223], s[30:31], 0, v[194:195]
	global_load_lds_dwordx4 v[220:221], off
	s_mov_b32 m0, s39
	v_lshl_add_u64 v[224:225], s[30:31], 0, v[198:199]
	global_load_lds_dwordx4 v[222:223], off
	s_mov_b32 m0, s44
	s_mov_b64 s[36:37], -1
	global_load_lds_dwordx4 v[224:225], off
	s_and_b64 vcc, exec, s[34:35]
	s_cbranch_vccz .Lpl1226_1232
	s_waitcnt vmcnt(8)
	s_mov_b64 s[36:37], 0

; #define PG8_WAIT_L(n) asm volatile("s_waitcnt lgkmcnt(" #n ")" ::: "memory")
; #define PG8_WAIT_V8R() do { if (relax) { if (GATHER && wid == 0 && has_next) asm volatile("s_waitcnt vmcnt(%0)" :: "n"(9 + Epi::NSTORES) : "memory"); else asm volatile("s_waitcnt vmcnt(%0)" :: "n"(8 + Epi::NSTORES) : "memory"); } else PG8_WAIT_V(8); } while (0)
; #define PG8_BAR __builtin_amdgcn_s_barrier()
; #define PG8_SCHED __builtin_amdgcn_sched_barrier(0)
; template <class Epi, class Sched, bool GATHER, bool FP8 = false>
; __device__ __forceinline__ void gemm_phase(LAS unsigned char* lds, LAS int* idx, const Gemm g, const Sched& S, const Epi& E) {
;     ...
;             PG8_WAIT_V8R(); PG8_WAIT_L(0); PG8_BAR; PG8_MMA(1, 0, At, B0); PG8_MMA(1, 1, At, B1); PG8_BAR; PG8_SCHED;
.Lpl1226_1225:
	s_waitcnt lgkmcnt(0)
	s_add_i32 s64, s64, 2
	s_barrier
	s_setprio 1
	s_waitcnt lgkmcnt(0)
	v_mfma_scale_f32_16x16x128_f8f6f4 v[126:129], v[26:33], v[58:65], 0, v246, v246 op_sel_hi:[0,0,0]
	v_mfma_scale_f32_16x16x128_f8f6f4 v[122:125], v[18:25], v[58:65], 0, v246, v246 op_sel_hi:[0,0,0]
	v_mfma_scale_f32_16x16x128_f8f6f4 v[110:113], v[26:33], v[50:57], 0, v246, v246 op_sel_hi:[0,0,0]
	v_mfma_scale_f32_16x16x128_f8f6f4 v[106:109], v[18:25], v[50:57], 0, v246, v246 op_sel_hi:[0,0,0]
	v_mfma_scale_f32_16x16x128_f8f6f4 v[94:97], v[26:33], v[42:49], 0, v246, v246 op_sel_hi:[0,0,0]
	v_mfma_scale_f32_16x16x128_f8f6f4 v[90:93], v[18:25], v[42:49], 0, v246, v246 op_sel_hi:[0,0,0]
	v_mfma_scale_f32_16x16x128_f8f6f4 v[78:81], v[26:33], v[34:41], 0, v246, v246 op_sel_hi:[0,0,0]
	v_mfma_scale_f32_16x16x128_f8f6f4 v[74:77], v[18:25], v[34:41], 0, v246, v246 op_sel_hi:[0,0,0]
	s_setprio 0
	s_setprio 1
	v_mfma_scale_f32_16x16x128_f8f6f4 v[118:121], v[10:17], v[58:65], 0, v246, v246 op_sel_hi:[0,0,0]
	v_mfma_scale_f32_16x16x128_f8f6f4 v[114:117], v[2:9], v[58:65], 0, v246, v246 op_sel_hi:[0,0,0]
	v_mfma_scale_f32_16x16x128_f8f6f4 v[102:105], v[10:17], v[50:57], 0, v246, v246 op_sel_hi:[0,0,0]
	v_mfma_scale_f32_16x16x128_f8f6f4 v[98:101], v[2:9], v[50:57], 0, v246, v246 op_sel_hi:[0,0,0]
	v_mfma_scale_f32_16x16x128_f8f6f4 v[86:89], v[10:17], v[42:49], 0, v246, v246 op_sel_hi:[0,0,0]
	v_mfma_scale_f32_16x16x128_f8f6f4 v[82:85], v[2:9], v[42:49], 0, v246, v246 op_sel_hi:[0,0,0]
	v_mfma_scale_f32_16x16x128_f8f6f4 v[70:73], v[10:17], v[34:41], 0, v246, v246 op_sel_hi:[0,0,0]
	v_mfma_scale_f32_16x16x128_f8f6f4 v[66:69], v[2:9], v[34:41], 0, v246, v246 op_sel_hi:[0,0,0]
	s_branch .Lpl1226_join
